# MoBA block gating: a candidate kmean row is read with its 8 ds_read_b128 issued together (into VGPRs that are dead during gating) and counted lgkmcnt waits, instead of 4 serialized read pairs; FMA ord
# speedup vs baseline: 1.0069x; 1.0069x over previous
.LBB0_470:
	s_or_b64 exec, exec, s[0:1]
	s_lshl_b32 s0, s56, 7
	s_lshr_b32 s33, s56, 8
	s_and_b32 s29, s0, 0x7800
	s_sub_i32 s30, 7, s33
	s_and_b32 s57, s56, 15
	s_mul_i32 s54, s29, 0x1800
	v_readlane_b32 s0, v254, 46
	v_readlane_b32 s1, v254, 47
	s_add_u32 s0, s0, s54
	s_addc_u32 s1, s1, 0
	s_lshl_b32 s55, s57, 7
	s_add_u32 s0, s0, s55
	s_addc_u32 s1, s1, 0
	s_lshl_b32 s6, s30, 8
	v_lshl_add_u64 v[0:1], s[0:1], 0, v[112:113]
	v_lshl_add_u64 v[4:5], s[0:1], 0, v[114:115]
	s_add_i32 s8, s6, s17
	v_lshl_add_u64 v[0:1], v[0:1], 0, s[10:11]
	s_mov_b64 s[6:7], 0x800
	v_lshl_add_u64 v[4:5], v[4:5], 0, s[12:13]
	v_lshl_add_u64 v[2:3], v[0:1], 0, s[6:7]
	v_lshl_add_u64 v[4:5], v[4:5], 0, v[116:117]
	s_mov_b64 s[6:7], 0x1000
	s_mov_b32 m0, s18
	v_lshl_add_u64 v[6:7], v[4:5], 0, s[6:7]
	global_load_lds_dwordx4 v[2:3], off
	s_mov_b32 m0, s20
	s_mov_b64 s[6:7], 0x60800
	global_load_lds_dwordx4 v[6:7], off
	v_lshl_add_u64 v[0:1], v[0:1], 0, s[6:7]
	s_mov_b32 m0, s21
	s_mov_b64 s[6:7], 0x61000
	global_load_lds_dwordx4 v[0:1], off
	v_lshl_add_u64 v[0:1], v[4:5], 0, s[6:7]
	s_mov_b32 m0, s22
	v_or_b32_e32 v195, s8, v161
	global_load_lds_dwordx4 v[0:1], off
	v_mov_b64_e32 v[0:1], s[0:1]
	v_mad_u64_u32 v[0:1], s[0:1], v195, s19, v[0:1]
	s_lshl_b32 s0, s56, 11
	v_lshl_add_u64 v[0:1], v[118:119], 1, v[0:1]
	s_and_b32 s0, s0, 0x7f800
	s_mov_b32 s1, s9
	global_load_dwordx4 v[76:79], v[0:1], off
	global_load_dwordx4 v[72:75], v[0:1], off offset:32
	global_load_dwordx4 v[68:71], v[0:1], off offset:64
	global_load_dwordx4 v[64:67], v[0:1], off offset:96
	v_lshl_add_u64 v[0:1], v[120:121], 0, s[0:1]
	global_load_dword v0, v[0:1], off
	s_cmp_eq_u32 s33, 7
	s_cselect_b64 s[0:1], -1, 0
	v_mov_b32_e32 v16, 0
	s_and_b64 vcc, exec, s[0:1]
	v_mov_b32_e32 v17, 0
	s_waitcnt vmcnt(0)
	v_lshlrev_b32_e32 v26, 16, v76
	v_and_b32_e32 v27, 0xffff0000, v76
	v_lshlrev_b32_e32 v28, 16, v77
	v_and_b32_e32 v29, 0xffff0000, v77
	v_lshlrev_b32_e32 v30, 16, v78
	ds_write_b32 v162, v0
	s_waitcnt vmcnt(0) lgkmcnt(0)
	s_barrier
	v_and_b32_e32 v31, 0xffff0000, v78
	v_lshlrev_b32_e32 v32, 16, v79
	v_and_b32_e32 v33, 0xffff0000, v79
	v_lshlrev_b32_e32 v18, 16, v72
	v_and_b32_e32 v19, 0xffff0000, v72
	v_lshlrev_b32_e32 v20, 16, v73
	v_and_b32_e32 v21, 0xffff0000, v73
	v_lshlrev_b32_e32 v22, 16, v74
	v_and_b32_e32 v23, 0xffff0000, v74
	v_lshlrev_b32_e32 v24, 16, v75
	v_and_b32_e32 v25, 0xffff0000, v75
	v_lshlrev_b32_e32 v15, 16, v68
	v_and_b32_e32 v14, 0xffff0000, v68
	v_lshlrev_b32_e32 v13, 16, v69
	v_and_b32_e32 v12, 0xffff0000, v69
	v_lshlrev_b32_e32 v8, 16, v70
	v_and_b32_e32 v9, 0xffff0000, v70
	v_lshlrev_b32_e32 v10, 16, v71
	v_and_b32_e32 v11, 0xffff0000, v71
	v_lshlrev_b32_e32 v7, 16, v64
	v_and_b32_e32 v6, 0xffff0000, v64
	v_lshlrev_b32_e32 v5, 16, v65
	v_and_b32_e32 v4, 0xffff0000, v65
	v_lshlrev_b32_e32 v3, 16, v66
	v_and_b32_e32 v2, 0xffff0000, v66
	v_lshlrev_b32_e32 v1, 16, v67
	v_and_b32_e32 v0, 0xffff0000, v67
	s_cbranch_vccnz .LBB0_472
	ds_read_b128 v[34:37], v163
	ds_read_b128 v[38:41], v163 offset:16
	ds_read_b128 v[136:139], v163 offset:64
	ds_read_b128 v[140:143], v163 offset:80
	ds_read_b128 v[144:147], v163 offset:128
	ds_read_b128 v[148:151], v163 offset:144
	ds_read_b128 v[152:155], v163 offset:192
	ds_read_b128 v[156:159], v163 offset:208
	s_waitcnt lgkmcnt(7)
	v_fma_f32 v17, v26, v34, 0
	v_fmac_f32_e32 v17, v27, v35
	v_fmac_f32_e32 v17, v28, v36
	v_fmac_f32_e32 v17, v29, v37
	s_waitcnt lgkmcnt(6)
	v_fmac_f32_e32 v17, v30, v38
	v_fmac_f32_e32 v17, v31, v39
	v_fmac_f32_e32 v17, v32, v40
	v_fmac_f32_e32 v17, v33, v41
	s_waitcnt lgkmcnt(5)
	v_fmac_f32_e32 v17, v18, v136
	v_fmac_f32_e32 v17, v19, v137
	v_fmac_f32_e32 v17, v20, v138
	v_fmac_f32_e32 v17, v21, v139
	s_waitcnt lgkmcnt(4)
	v_fmac_f32_e32 v17, v22, v140
	v_fmac_f32_e32 v17, v23, v141
	v_fmac_f32_e32 v17, v24, v142
	v_fmac_f32_e32 v17, v25, v143
	s_waitcnt lgkmcnt(3)
	v_fmac_f32_e32 v17, v15, v144
	v_fmac_f32_e32 v17, v14, v145
	v_fmac_f32_e32 v17, v13, v146
	v_fmac_f32_e32 v17, v12, v147
	s_waitcnt lgkmcnt(2)
	v_fmac_f32_e32 v17, v8, v148
	v_fmac_f32_e32 v17, v9, v149
	v_fmac_f32_e32 v17, v10, v150
	v_fmac_f32_e32 v17, v11, v151
	s_waitcnt lgkmcnt(1)
	v_fmac_f32_e32 v17, v7, v152
	v_fmac_f32_e32 v17, v6, v153
	v_fmac_f32_e32 v17, v5, v154
	v_fmac_f32_e32 v17, v4, v155
	s_waitcnt lgkmcnt(0)
	v_fmac_f32_e32 v17, v3, v156
	v_fmac_f32_e32 v17, v2, v157
	v_fmac_f32_e32 v17, v1, v158
	v_fmac_f32_e32 v17, v0, v159
	v_mov_b32_e32 v34, v17
	s_nop 1
	v_permlane32_swap_b32_e32 v17, v34
	v_add_f32_e32 v17, v17, v34
.LBB0_472:
	s_cmpk_lt_u32 s56, 0x600
	s_cselect_b64 s[6:7], -1, 0
	s_cmpk_gt_u32 s56, 0x5ff
	s_cbranch_scc1 .LBB0_474
	ds_read_b128 v[34:37], v163 offset:256
	ds_read_b128 v[38:41], v163 offset:272
	ds_read_b128 v[136:139], v163 offset:320
	ds_read_b128 v[140:143], v163 offset:336
	ds_read_b128 v[144:147], v163 offset:384
	ds_read_b128 v[148:151], v163 offset:400
	ds_read_b128 v[152:155], v163 offset:448
	ds_read_b128 v[156:159], v163 offset:464
	s_waitcnt lgkmcnt(7)
	v_fma_f32 v16, v26, v34, 0
	v_fmac_f32_e32 v16, v27, v35
	v_fmac_f32_e32 v16, v28, v36
	v_fmac_f32_e32 v16, v29, v37
	s_waitcnt lgkmcnt(6)
	v_fmac_f32_e32 v16, v30, v38
	v_fmac_f32_e32 v16, v31, v39
	v_fmac_f32_e32 v16, v32, v40
	v_fmac_f32_e32 v16, v33, v41
	s_waitcnt lgkmcnt(5)
	v_fmac_f32_e32 v16, v18, v136
	v_fmac_f32_e32 v16, v19, v137
	v_fmac_f32_e32 v16, v20, v138
	v_fmac_f32_e32 v16, v21, v139
	s_waitcnt lgkmcnt(4)
	v_fmac_f32_e32 v16, v22, v140
	v_fmac_f32_e32 v16, v23, v141
	v_fmac_f32_e32 v16, v24, v142
	v_fmac_f32_e32 v16, v25, v143
	s_waitcnt lgkmcnt(3)
	v_fmac_f32_e32 v16, v15, v144
	v_fmac_f32_e32 v16, v14, v145
	v_fmac_f32_e32 v16, v13, v146
	v_fmac_f32_e32 v16, v12, v147
	s_waitcnt lgkmcnt(2)
	v_fmac_f32_e32 v16, v8, v148
	v_fmac_f32_e32 v16, v9, v149
	v_fmac_f32_e32 v16, v10, v150
	v_fmac_f32_e32 v16, v11, v151
	s_waitcnt lgkmcnt(1)
	v_fmac_f32_e32 v16, v7, v152
	v_fmac_f32_e32 v16, v6, v153
	v_fmac_f32_e32 v16, v5, v154
	v_fmac_f32_e32 v16, v4, v155
	s_waitcnt lgkmcnt(0)
	v_fmac_f32_e32 v16, v3, v156
	v_fmac_f32_e32 v16, v2, v157
	v_fmac_f32_e32 v16, v1, v158
	v_fmac_f32_e32 v16, v0, v159
	v_mov_b32_e32 v34, v16
	s_nop 1
	v_permlane32_swap_b32_e32 v16, v34
	v_add_f32_e32 v16, v16, v34
.LBB0_474:
	s_cmpk_lt_u32 s56, 0x500
	v_mov_b32_e32 v34, 0
	s_cselect_b64 s[44:45], -1, 0
	s_cmpk_gt_u32 s56, 0x4ff
	v_mov_b32_e32 v35, 0
	s_cbranch_scc1 .LBB0_476
	ds_read_b128 v[36:39], v163 offset:512
	ds_read_b128 v[40:43], v163 offset:528
	ds_read_b128 v[136:139], v163 offset:576
	ds_read_b128 v[140:143], v163 offset:592
	ds_read_b128 v[144:147], v163 offset:640
	ds_read_b128 v[148:151], v163 offset:656
	ds_read_b128 v[152:155], v163 offset:704
	ds_read_b128 v[156:159], v163 offset:720
	s_waitcnt lgkmcnt(7)
	v_fma_f32 v35, v26, v36, 0
	v_fmac_f32_e32 v35, v27, v37
	v_fmac_f32_e32 v35, v28, v38
	v_fmac_f32_e32 v35, v29, v39
	s_waitcnt lgkmcnt(6)
	v_fmac_f32_e32 v35, v30, v40
	v_fmac_f32_e32 v35, v31, v41
	v_fmac_f32_e32 v35, v32, v42
	v_fmac_f32_e32 v35, v33, v43
	s_waitcnt lgkmcnt(5)
	v_fmac_f32_e32 v35, v18, v136
	v_fmac_f32_e32 v35, v19, v137
	v_fmac_f32_e32 v35, v20, v138
	v_fmac_f32_e32 v35, v21, v139
	s_waitcnt lgkmcnt(4)
	v_fmac_f32_e32 v35, v22, v140
	v_fmac_f32_e32 v35, v23, v141
	v_fmac_f32_e32 v35, v24, v142
	v_fmac_f32_e32 v35, v25, v143
	s_waitcnt lgkmcnt(3)
	v_fmac_f32_e32 v35, v15, v144
	v_fmac_f32_e32 v35, v14, v145
	v_fmac_f32_e32 v35, v13, v146
	v_fmac_f32_e32 v35, v12, v147
	s_waitcnt lgkmcnt(2)
	v_fmac_f32_e32 v35, v8, v148
	v_fmac_f32_e32 v35, v9, v149
	v_fmac_f32_e32 v35, v10, v150
	v_fmac_f32_e32 v35, v11, v151
	s_waitcnt lgkmcnt(1)
	v_fmac_f32_e32 v35, v7, v152
	v_fmac_f32_e32 v35, v6, v153
	v_fmac_f32_e32 v35, v5, v154
	v_fmac_f32_e32 v35, v4, v155
	s_waitcnt lgkmcnt(0)
	v_fmac_f32_e32 v35, v3, v156
	v_fmac_f32_e32 v35, v2, v157
	v_fmac_f32_e32 v35, v1, v158
	v_fmac_f32_e32 v35, v0, v159
	v_mov_b32_e32 v36, v35
	s_nop 1
	v_permlane32_swap_b32_e32 v35, v36
	v_add_f32_e32 v35, v35, v36
.LBB0_476:
	s_cmpk_lt_u32 s56, 0x400
	s_cselect_b64 s[46:47], -1, 0
	s_cmpk_gt_u32 s56, 0x3ff
	s_cbranch_scc1 .LBB0_478
	ds_read_b128 v[36:39], v163 offset:768
	ds_read_b128 v[40:43], v163 offset:784
	ds_read_b128 v[136:139], v163 offset:832
	ds_read_b128 v[140:143], v163 offset:848
	ds_read_b128 v[144:147], v163 offset:896
	ds_read_b128 v[148:151], v163 offset:912
	ds_read_b128 v[152:155], v163 offset:960
	ds_read_b128 v[156:159], v163 offset:976
	s_waitcnt lgkmcnt(7)
	v_fma_f32 v34, v26, v36, 0
	v_fmac_f32_e32 v34, v27, v37
	v_fmac_f32_e32 v34, v28, v38
	v_fmac_f32_e32 v34, v29, v39
	s_waitcnt lgkmcnt(6)
	v_fmac_f32_e32 v34, v30, v40
	v_fmac_f32_e32 v34, v31, v41
	v_fmac_f32_e32 v34, v32, v42
	v_fmac_f32_e32 v34, v33, v43
	s_waitcnt lgkmcnt(5)
	v_fmac_f32_e32 v34, v18, v136
	v_fmac_f32_e32 v34, v19, v137
	v_fmac_f32_e32 v34, v20, v138
	v_fmac_f32_e32 v34, v21, v139
	s_waitcnt lgkmcnt(4)
	v_fmac_f32_e32 v34, v22, v140
	v_fmac_f32_e32 v34, v23, v141
	v_fmac_f32_e32 v34, v24, v142
	v_fmac_f32_e32 v34, v25, v143
	s_waitcnt lgkmcnt(3)
	v_fmac_f32_e32 v34, v15, v144
	v_fmac_f32_e32 v34, v14, v145
	v_fmac_f32_e32 v34, v13, v146
	v_fmac_f32_e32 v34, v12, v147
	s_waitcnt lgkmcnt(2)
	v_fmac_f32_e32 v34, v8, v148
	v_fmac_f32_e32 v34, v9, v149
	v_fmac_f32_e32 v34, v10, v150
	v_fmac_f32_e32 v34, v11, v151
	s_waitcnt lgkmcnt(1)
	v_fmac_f32_e32 v34, v7, v152
	v_fmac_f32_e32 v34, v6, v153
	v_fmac_f32_e32 v34, v5, v154
	v_fmac_f32_e32 v34, v4, v155
	s_waitcnt lgkmcnt(0)
	v_fmac_f32_e32 v34, v3, v156
	v_fmac_f32_e32 v34, v2, v157
	v_fmac_f32_e32 v34, v1, v158
	v_fmac_f32_e32 v34, v0, v159
	v_mov_b32_e32 v36, v34
	s_nop 1
	v_permlane32_swap_b32_e32 v34, v36
	v_add_f32_e32 v34, v34, v36
.LBB0_478:
	s_cmpk_lt_u32 s56, 0x300
	v_mov_b32_e32 v36, 0
	s_cselect_b64 s[48:49], -1, 0
	s_cmpk_gt_u32 s56, 0x2ff
	v_mov_b32_e32 v37, 0
	s_cbranch_scc1 .LBB0_480
	ds_read_b128 v[38:41], v163 offset:1024
	ds_read_b128 v[42:45], v163 offset:1040
	ds_read_b128 v[136:139], v163 offset:1088
	ds_read_b128 v[140:143], v163 offset:1104
	ds_read_b128 v[144:147], v163 offset:1152
	ds_read_b128 v[148:151], v163 offset:1168
	ds_read_b128 v[152:155], v163 offset:1216
	ds_read_b128 v[156:159], v163 offset:1232
	s_waitcnt lgkmcnt(7)
	v_fma_f32 v37, v26, v38, 0
	v_fmac_f32_e32 v37, v27, v39
	v_fmac_f32_e32 v37, v28, v40
	v_fmac_f32_e32 v37, v29, v41
	s_waitcnt lgkmcnt(6)
	v_fmac_f32_e32 v37, v30, v42
	v_fmac_f32_e32 v37, v31, v43
	v_fmac_f32_e32 v37, v32, v44
	v_fmac_f32_e32 v37, v33, v45
	s_waitcnt lgkmcnt(5)
	v_fmac_f32_e32 v37, v18, v136
	v_fmac_f32_e32 v37, v19, v137
	v_fmac_f32_e32 v37, v20, v138
	v_fmac_f32_e32 v37, v21, v139
	s_waitcnt lgkmcnt(4)
	v_fmac_f32_e32 v37, v22, v140
	v_fmac_f32_e32 v37, v23, v141
	v_fmac_f32_e32 v37, v24, v142
	v_fmac_f32_e32 v37, v25, v143
	s_waitcnt lgkmcnt(3)
	v_fmac_f32_e32 v37, v15, v144
	v_fmac_f32_e32 v37, v14, v145
	v_fmac_f32_e32 v37, v13, v146
	v_fmac_f32_e32 v37, v12, v147
	s_waitcnt lgkmcnt(2)
	v_fmac_f32_e32 v37, v8, v148
	v_fmac_f32_e32 v37, v9, v149
	v_fmac_f32_e32 v37, v10, v150
	v_fmac_f32_e32 v37, v11, v151
	s_waitcnt lgkmcnt(1)
	v_fmac_f32_e32 v37, v7, v152
	v_fmac_f32_e32 v37, v6, v153
	v_fmac_f32_e32 v37, v5, v154
	v_fmac_f32_e32 v37, v4, v155
	s_waitcnt lgkmcnt(0)
	v_fmac_f32_e32 v37, v3, v156
	v_fmac_f32_e32 v37, v2, v157
	v_fmac_f32_e32 v37, v1, v158
	v_fmac_f32_e32 v37, v0, v159
	v_mov_b32_e32 v38, v37
	s_nop 1
	v_permlane32_swap_b32_e32 v37, v38
	v_add_f32_e32 v37, v37, v38
.LBB0_480:
	s_cmpk_lt_u32 s56, 0x200
	s_cselect_b64 s[50:51], -1, 0
	s_cmpk_gt_u32 s56, 0x1ff
	s_cbranch_scc1 .LBB0_482
	ds_read_b128 v[38:41], v163 offset:1280
	ds_read_b128 v[42:45], v163 offset:1296
	ds_read_b128 v[136:139], v163 offset:1344
	ds_read_b128 v[140:143], v163 offset:1360
	ds_read_b128 v[144:147], v163 offset:1408
	ds_read_b128 v[148:151], v163 offset:1424
	ds_read_b128 v[152:155], v163 offset:1472
	ds_read_b128 v[156:159], v163 offset:1488
	s_waitcnt lgkmcnt(7)
	v_fma_f32 v36, v26, v38, 0
	v_fmac_f32_e32 v36, v27, v39
	v_fmac_f32_e32 v36, v28, v40
	v_fmac_f32_e32 v36, v29, v41
	s_waitcnt lgkmcnt(6)
	v_fmac_f32_e32 v36, v30, v42
	v_fmac_f32_e32 v36, v31, v43
	v_fmac_f32_e32 v36, v32, v44
	v_fmac_f32_e32 v36, v33, v45
	s_waitcnt lgkmcnt(5)
	v_fmac_f32_e32 v36, v18, v136
	v_fmac_f32_e32 v36, v19, v137
	v_fmac_f32_e32 v36, v20, v138
	v_fmac_f32_e32 v36, v21, v139
	s_waitcnt lgkmcnt(4)
	v_fmac_f32_e32 v36, v22, v140
	v_fmac_f32_e32 v36, v23, v141
	v_fmac_f32_e32 v36, v24, v142
	v_fmac_f32_e32 v36, v25, v143
	s_waitcnt lgkmcnt(3)
	v_fmac_f32_e32 v36, v15, v144
	v_fmac_f32_e32 v36, v14, v145
	v_fmac_f32_e32 v36, v13, v146
	v_fmac_f32_e32 v36, v12, v147
	s_waitcnt lgkmcnt(2)
	v_fmac_f32_e32 v36, v8, v148
	v_fmac_f32_e32 v36, v9, v149
	v_fmac_f32_e32 v36, v10, v150
	v_fmac_f32_e32 v36, v11, v151
	s_waitcnt lgkmcnt(1)
	v_fmac_f32_e32 v36, v7, v152
	v_fmac_f32_e32 v36, v6, v153
	v_fmac_f32_e32 v36, v5, v154
	v_fmac_f32_e32 v36, v4, v155
	s_waitcnt lgkmcnt(0)
	v_fmac_f32_e32 v36, v3, v156
	v_fmac_f32_e32 v36, v2, v157
	v_fmac_f32_e32 v36, v1, v158
	v_fmac_f32_e32 v36, v0, v159
	v_mov_b32_e32 v38, v36
	s_nop 1
	v_permlane32_swap_b32_e32 v36, v38
	v_add_f32_e32 v36, v36, v38
.LBB0_482:
	s_lshl_b32 s31, s57, 6
	s_cmpk_lt_u32 s56, 0x100
	v_mov_b32_e32 v197, 0
	s_cselect_b64 s[52:53], -1, 0
	s_cmpk_gt_u32 s56, 0xff
	v_mov_b32_e32 v38, 0
	s_cbranch_scc1 .LBB0_484
	ds_read_b128 v[38:41], v163 offset:1536
	ds_read_b128 v[42:45], v163 offset:1552
	ds_read_b128 v[136:139], v163 offset:1600
	ds_read_b128 v[140:143], v163 offset:1616
	ds_read_b128 v[144:147], v163 offset:1664
	ds_read_b128 v[148:151], v163 offset:1680
	ds_read_b128 v[152:155], v163 offset:1728
	ds_read_b128 v[156:159], v163 offset:1744
	s_waitcnt lgkmcnt(7)
	v_fma_f32 v38, v26, v38, 0
	v_fmac_f32_e32 v38, v27, v39
	v_fmac_f32_e32 v38, v28, v40
	v_fmac_f32_e32 v38, v29, v41
	s_waitcnt lgkmcnt(6)
	v_fmac_f32_e32 v38, v30, v42
	v_fmac_f32_e32 v38, v31, v43
	v_fmac_f32_e32 v38, v32, v44
	v_fmac_f32_e32 v38, v33, v45
	s_waitcnt lgkmcnt(5)
	v_fmac_f32_e32 v38, v18, v136
	v_fmac_f32_e32 v38, v19, v137
	v_fmac_f32_e32 v38, v20, v138
	v_fmac_f32_e32 v38, v21, v139
	s_waitcnt lgkmcnt(4)
	v_fmac_f32_e32 v38, v22, v140
	v_fmac_f32_e32 v38, v23, v141
	v_fmac_f32_e32 v38, v24, v142
	v_fmac_f32_e32 v38, v25, v143
	s_waitcnt lgkmcnt(3)
	v_fmac_f32_e32 v38, v15, v144
	v_fmac_f32_e32 v38, v14, v145
	v_fmac_f32_e32 v38, v13, v146
	v_fmac_f32_e32 v38, v12, v147
	s_waitcnt lgkmcnt(2)
	v_fmac_f32_e32 v38, v8, v148
	v_fmac_f32_e32 v38, v9, v149
	v_fmac_f32_e32 v38, v10, v150
	v_fmac_f32_e32 v38, v11, v151
	s_waitcnt lgkmcnt(1)
	v_fmac_f32_e32 v38, v7, v152
	v_fmac_f32_e32 v38, v6, v153
	v_fmac_f32_e32 v38, v5, v154
	v_fmac_f32_e32 v38, v4, v155
	s_waitcnt lgkmcnt(0)
	v_fmac_f32_e32 v38, v3, v156
	v_fmac_f32_e32 v38, v2, v157
	v_fmac_f32_e32 v38, v1, v158
	v_fmac_f32_e32 v38, v0, v159
	v_mov_b32_e32 v0, v38
	s_nop 1
	v_permlane32_swap_b32_e32 v38, v0
	v_add_f32_e32 v38, v38, v0

.LBB0_3009:
	s_or_b64 exec, exec, s[0:1]
	s_lshl_b32 s0, s56, 7
	s_lshr_b32 s53, s56, 8
	s_and_b32 s50, s0, 0x7800
	s_sub_i32 s52, 7, s53
	s_and_b32 s57, s56, 15
	s_mul_i32 s54, s50, 0x1800
	v_readlane_b32 s0, v254, 46
	v_readlane_b32 s1, v254, 47
	s_add_u32 s0, s0, s54
	s_addc_u32 s1, s1, 0
	s_lshl_b32 s55, s57, 7
	s_add_u32 s0, s0, s55
	s_addc_u32 s1, s1, 0
	s_lshl_b32 s6, s52, 8
	s_add_i32 s8, s6, s42
	s_lshl_b32 s6, s56, 11
	s_and_b32 s6, s6, 0x7f800
	s_mov_b32 s7, s9
	v_lshl_add_u64 v[2:3], v[120:121], 0, s[6:7]
	global_load_dword v10, v[2:3], off
	v_lshl_add_u64 v[2:3], s[0:1], 0, v[112:113]
	v_or_b32_e32 v195, s8, v161
	v_mov_b64_e32 v[0:1], s[0:1]
	v_lshl_add_u64 v[4:5], s[0:1], 0, v[114:115]
	v_lshl_add_u64 v[2:3], v[2:3], 0, s[10:11]
	s_mov_b64 s[0:1], 0x800
	v_mad_u64_u32 v[0:1], s[6:7], v195, s44, v[0:1]
	v_lshl_add_u64 v[4:5], v[4:5], 0, s[12:13]
	v_lshl_add_u64 v[6:7], v[2:3], 0, s[0:1]
	s_mov_b64 s[0:1], 0x60800
	s_mov_b32 m0, s43
	v_lshl_add_u64 v[0:1], v[118:119], 1, v[0:1]
	v_lshl_add_u64 v[4:5], v[4:5], 0, v[116:117]
	v_lshl_add_u64 v[2:3], v[2:3], 0, s[0:1]
	s_mov_b64 s[0:1], 0x1000
	global_load_dwordx4 v[76:79], v[0:1], off
	global_load_dwordx4 v[72:75], v[0:1], off offset:32
	v_lshl_add_u64 v[8:9], v[4:5], 0, s[0:1]
	global_load_lds_dwordx4 v[6:7], off
	s_mov_b32 m0, s45
	global_load_dwordx4 v[68:71], v[0:1], off offset:64
	global_load_dwordx4 v[64:67], v[0:1], off offset:96
	s_mov_b64 s[0:1], 0x61000
	global_load_lds_dwordx4 v[8:9], off
	s_mov_b32 m0, s46
	v_lshl_add_u64 v[0:1], v[4:5], 0, s[0:1]
	global_load_lds_dwordx4 v[2:3], off
	s_mov_b32 m0, s47
	s_cmp_eq_u32 s53, 7
	global_load_lds_dwordx4 v[0:1], off
	s_cselect_b64 s[0:1], -1, 0
	v_mov_b32_e32 v0, 0
	s_and_b64 vcc, exec, s[0:1]
	v_mov_b32_e32 v1, 0
	s_waitcnt vmcnt(0)
	ds_write_b32 v162, v10
	s_waitcnt vmcnt(0) lgkmcnt(0)
	s_barrier
	v_lshlrev_b32_e32 v28, 16, v76
	v_and_b32_e32 v29, 0xffff0000, v76
	v_lshlrev_b32_e32 v30, 16, v77
	v_and_b32_e32 v31, 0xffff0000, v77
	v_lshlrev_b32_e32 v32, 16, v78
	v_and_b32_e32 v33, 0xffff0000, v78
	v_lshlrev_b32_e32 v34, 16, v79
	v_and_b32_e32 v35, 0xffff0000, v79
	v_lshlrev_b32_e32 v18, 16, v72
	v_and_b32_e32 v19, 0xffff0000, v72
	v_lshlrev_b32_e32 v20, 16, v73
	v_and_b32_e32 v21, 0xffff0000, v73
	v_lshlrev_b32_e32 v22, 16, v74
	v_and_b32_e32 v23, 0xffff0000, v74
	v_lshlrev_b32_e32 v24, 16, v75
	v_and_b32_e32 v25, 0xffff0000, v75
	v_lshlrev_b32_e32 v17, 16, v68
	v_and_b32_e32 v16, 0xffff0000, v68
	v_lshlrev_b32_e32 v15, 16, v69
	v_and_b32_e32 v14, 0xffff0000, v69
	v_lshlrev_b32_e32 v10, 16, v70
	v_and_b32_e32 v11, 0xffff0000, v70
	v_lshlrev_b32_e32 v12, 16, v71
	v_and_b32_e32 v13, 0xffff0000, v71
	v_lshlrev_b32_e32 v9, 16, v64
	v_and_b32_e32 v8, 0xffff0000, v64
	v_lshlrev_b32_e32 v7, 16, v65
	v_and_b32_e32 v6, 0xffff0000, v65
	v_lshlrev_b32_e32 v5, 16, v66
	v_and_b32_e32 v4, 0xffff0000, v66
	v_lshlrev_b32_e32 v3, 16, v67
	v_and_b32_e32 v2, 0xffff0000, v67
	s_cbranch_vccnz .LBB0_3011
	ds_read_b128 v[36:39], v163
	ds_read_b128 v[40:43], v163 offset:16
	ds_read_b128 v[136:139], v163 offset:64
	ds_read_b128 v[140:143], v163 offset:80
	ds_read_b128 v[144:147], v163 offset:128
	ds_read_b128 v[148:151], v163 offset:144
	ds_read_b128 v[152:155], v163 offset:192
	ds_read_b128 v[156:159], v163 offset:208
	s_waitcnt lgkmcnt(7)
	v_fma_f32 v1, v28, v36, 0
	v_fmac_f32_e32 v1, v29, v37
	v_fmac_f32_e32 v1, v30, v38
	v_fmac_f32_e32 v1, v31, v39
	s_waitcnt lgkmcnt(6)
	v_fmac_f32_e32 v1, v32, v40
	v_fmac_f32_e32 v1, v33, v41
	v_fmac_f32_e32 v1, v34, v42
	v_fmac_f32_e32 v1, v35, v43
	s_waitcnt lgkmcnt(5)
	v_fmac_f32_e32 v1, v18, v136
	v_fmac_f32_e32 v1, v19, v137
	v_fmac_f32_e32 v1, v20, v138
	v_fmac_f32_e32 v1, v21, v139
	s_waitcnt lgkmcnt(4)
	v_fmac_f32_e32 v1, v22, v140
	v_fmac_f32_e32 v1, v23, v141
	v_fmac_f32_e32 v1, v24, v142
	v_fmac_f32_e32 v1, v25, v143
	s_waitcnt lgkmcnt(3)
	v_fmac_f32_e32 v1, v17, v144
	v_fmac_f32_e32 v1, v16, v145
	v_fmac_f32_e32 v1, v15, v146
	v_fmac_f32_e32 v1, v14, v147
	s_waitcnt lgkmcnt(2)
	v_fmac_f32_e32 v1, v10, v148
	v_fmac_f32_e32 v1, v11, v149
	v_fmac_f32_e32 v1, v12, v150
	v_fmac_f32_e32 v1, v13, v151
	s_waitcnt lgkmcnt(1)
	v_fmac_f32_e32 v1, v9, v152
	v_fmac_f32_e32 v1, v8, v153
	v_fmac_f32_e32 v1, v7, v154
	v_fmac_f32_e32 v1, v6, v155
	s_waitcnt lgkmcnt(0)
	v_fmac_f32_e32 v1, v5, v156
	v_fmac_f32_e32 v1, v4, v157
	v_fmac_f32_e32 v1, v3, v158
	v_fmac_f32_e32 v1, v2, v159
	v_mov_b32_e32 v26, v1
	s_nop 1
	v_permlane32_swap_b32_e32 v1, v26
	v_add_f32_e32 v1, v1, v26
.LBB0_3011:
	s_cmpk_lt_u32 s56, 0x600
	s_cselect_b64 s[6:7], -1, 0
	s_cmpk_gt_u32 s56, 0x5ff
	s_cbranch_scc1 .LBB0_3013
	ds_read_b128 v[36:39], v163 offset:256
	ds_read_b128 v[40:43], v163 offset:272
	ds_read_b128 v[136:139], v163 offset:320
	ds_read_b128 v[140:143], v163 offset:336
	ds_read_b128 v[144:147], v163 offset:384
	ds_read_b128 v[148:151], v163 offset:400
	ds_read_b128 v[152:155], v163 offset:448
	ds_read_b128 v[156:159], v163 offset:464
	s_waitcnt lgkmcnt(7)
	v_fma_f32 v0, v28, v36, 0
	v_fmac_f32_e32 v0, v29, v37
	v_fmac_f32_e32 v0, v30, v38
	v_fmac_f32_e32 v0, v31, v39
	s_waitcnt lgkmcnt(6)
	v_fmac_f32_e32 v0, v32, v40
	v_fmac_f32_e32 v0, v33, v41
	v_fmac_f32_e32 v0, v34, v42
	v_fmac_f32_e32 v0, v35, v43
	s_waitcnt lgkmcnt(5)
	v_fmac_f32_e32 v0, v18, v136
	v_fmac_f32_e32 v0, v19, v137
	v_fmac_f32_e32 v0, v20, v138
	v_fmac_f32_e32 v0, v21, v139
	s_waitcnt lgkmcnt(4)
	v_fmac_f32_e32 v0, v22, v140
	v_fmac_f32_e32 v0, v23, v141
	v_fmac_f32_e32 v0, v24, v142
	v_fmac_f32_e32 v0, v25, v143
	s_waitcnt lgkmcnt(3)
	v_fmac_f32_e32 v0, v17, v144
	v_fmac_f32_e32 v0, v16, v145
	v_fmac_f32_e32 v0, v15, v146
	v_fmac_f32_e32 v0, v14, v147
	s_waitcnt lgkmcnt(2)
	v_fmac_f32_e32 v0, v10, v148
	v_fmac_f32_e32 v0, v11, v149
	v_fmac_f32_e32 v0, v12, v150
	v_fmac_f32_e32 v0, v13, v151
	s_waitcnt lgkmcnt(1)
	v_fmac_f32_e32 v0, v9, v152
	v_fmac_f32_e32 v0, v8, v153
	v_fmac_f32_e32 v0, v7, v154
	v_fmac_f32_e32 v0, v6, v155
	s_waitcnt lgkmcnt(0)
	v_fmac_f32_e32 v0, v5, v156
	v_fmac_f32_e32 v0, v4, v157
	v_fmac_f32_e32 v0, v3, v158
	v_fmac_f32_e32 v0, v2, v159
	v_mov_b32_e32 v26, v0
	s_nop 1
	v_permlane32_swap_b32_e32 v0, v26
	v_add_f32_e32 v0, v0, v26
.LBB0_3013:
	s_cmpk_lt_u32 s56, 0x500
	v_mov_b32_e32 v26, 0
	s_cselect_b64 s[30:31], -1, 0
	s_cmpk_gt_u32 s56, 0x4ff
	v_mov_b32_e32 v27, 0
	s_cbranch_scc1 .LBB0_3015
	ds_read_b128 v[36:39], v163 offset:512
	ds_read_b128 v[40:43], v163 offset:528
	ds_read_b128 v[136:139], v163 offset:576
	ds_read_b128 v[140:143], v163 offset:592
	ds_read_b128 v[144:147], v163 offset:640
	ds_read_b128 v[148:151], v163 offset:656
	ds_read_b128 v[152:155], v163 offset:704
	ds_read_b128 v[156:159], v163 offset:720
	s_waitcnt lgkmcnt(7)
	v_fma_f32 v27, v28, v36, 0
	v_fmac_f32_e32 v27, v29, v37
	v_fmac_f32_e32 v27, v30, v38
	v_fmac_f32_e32 v27, v31, v39
	s_waitcnt lgkmcnt(6)
	v_fmac_f32_e32 v27, v32, v40
	v_fmac_f32_e32 v27, v33, v41
	v_fmac_f32_e32 v27, v34, v42
	v_fmac_f32_e32 v27, v35, v43
	s_waitcnt lgkmcnt(5)
	v_fmac_f32_e32 v27, v18, v136
	v_fmac_f32_e32 v27, v19, v137
	v_fmac_f32_e32 v27, v20, v138
	v_fmac_f32_e32 v27, v21, v139
	s_waitcnt lgkmcnt(4)
	v_fmac_f32_e32 v27, v22, v140
	v_fmac_f32_e32 v27, v23, v141
	v_fmac_f32_e32 v27, v24, v142
	v_fmac_f32_e32 v27, v25, v143
	s_waitcnt lgkmcnt(3)
	v_fmac_f32_e32 v27, v17, v144
	v_fmac_f32_e32 v27, v16, v145
	v_fmac_f32_e32 v27, v15, v146
	v_fmac_f32_e32 v27, v14, v147
	s_waitcnt lgkmcnt(2)
	v_fmac_f32_e32 v27, v10, v148
	v_fmac_f32_e32 v27, v11, v149
	v_fmac_f32_e32 v27, v12, v150
	v_fmac_f32_e32 v27, v13, v151
	s_waitcnt lgkmcnt(1)
	v_fmac_f32_e32 v27, v9, v152
	v_fmac_f32_e32 v27, v8, v153
	v_fmac_f32_e32 v27, v7, v154
	v_fmac_f32_e32 v27, v6, v155
	s_waitcnt lgkmcnt(0)
	v_fmac_f32_e32 v27, v5, v156
	v_fmac_f32_e32 v27, v4, v157
	v_fmac_f32_e32 v27, v3, v158
	v_fmac_f32_e32 v27, v2, v159
	v_mov_b32_e32 v36, v27
	s_nop 1
	v_permlane32_swap_b32_e32 v27, v36
	v_add_f32_e32 v27, v27, v36
.LBB0_3015:
	s_cmpk_lt_u32 s56, 0x400
	s_cselect_b64 s[34:35], -1, 0
	s_cmpk_gt_u32 s56, 0x3ff
	s_cbranch_scc1 .LBB0_3017
	ds_read_b128 v[36:39], v163 offset:768
	ds_read_b128 v[40:43], v163 offset:784
	ds_read_b128 v[136:139], v163 offset:832
	ds_read_b128 v[140:143], v163 offset:848
	ds_read_b128 v[144:147], v163 offset:896
	ds_read_b128 v[148:151], v163 offset:912
	ds_read_b128 v[152:155], v163 offset:960
	ds_read_b128 v[156:159], v163 offset:976
	s_waitcnt lgkmcnt(7)
	v_fma_f32 v26, v28, v36, 0
	v_fmac_f32_e32 v26, v29, v37
	v_fmac_f32_e32 v26, v30, v38
	v_fmac_f32_e32 v26, v31, v39
	s_waitcnt lgkmcnt(6)
	v_fmac_f32_e32 v26, v32, v40
	v_fmac_f32_e32 v26, v33, v41
	v_fmac_f32_e32 v26, v34, v42
	v_fmac_f32_e32 v26, v35, v43
	s_waitcnt lgkmcnt(5)
	v_fmac_f32_e32 v26, v18, v136
	v_fmac_f32_e32 v26, v19, v137
	v_fmac_f32_e32 v26, v20, v138
	v_fmac_f32_e32 v26, v21, v139
	s_waitcnt lgkmcnt(4)
	v_fmac_f32_e32 v26, v22, v140
	v_fmac_f32_e32 v26, v23, v141
	v_fmac_f32_e32 v26, v24, v142
	v_fmac_f32_e32 v26, v25, v143
	s_waitcnt lgkmcnt(3)
	v_fmac_f32_e32 v26, v17, v144
	v_fmac_f32_e32 v26, v16, v145
	v_fmac_f32_e32 v26, v15, v146
	v_fmac_f32_e32 v26, v14, v147
	s_waitcnt lgkmcnt(2)
	v_fmac_f32_e32 v26, v10, v148
	v_fmac_f32_e32 v26, v11, v149
	v_fmac_f32_e32 v26, v12, v150
	v_fmac_f32_e32 v26, v13, v151
	s_waitcnt lgkmcnt(1)
	v_fmac_f32_e32 v26, v9, v152
	v_fmac_f32_e32 v26, v8, v153
	v_fmac_f32_e32 v26, v7, v154
	v_fmac_f32_e32 v26, v6, v155
	s_waitcnt lgkmcnt(0)
	v_fmac_f32_e32 v26, v5, v156
	v_fmac_f32_e32 v26, v4, v157
	v_fmac_f32_e32 v26, v3, v158
	v_fmac_f32_e32 v26, v2, v159
	v_mov_b32_e32 v36, v26
	s_nop 1
	v_permlane32_swap_b32_e32 v26, v36
	v_add_f32_e32 v26, v26, v36
.LBB0_3017:
	s_cmpk_lt_u32 s56, 0x300
	v_mov_b32_e32 v36, 0
	s_cselect_b64 s[36:37], -1, 0
	s_cmpk_gt_u32 s56, 0x2ff
	v_mov_b32_e32 v37, 0
	s_cbranch_scc1 .LBB0_3019
	ds_read_b128 v[38:41], v163 offset:1024
	ds_read_b128 v[42:45], v163 offset:1040
	ds_read_b128 v[136:139], v163 offset:1088
	ds_read_b128 v[140:143], v163 offset:1104
	ds_read_b128 v[144:147], v163 offset:1152
	ds_read_b128 v[148:151], v163 offset:1168
	ds_read_b128 v[152:155], v163 offset:1216
	ds_read_b128 v[156:159], v163 offset:1232
	s_waitcnt lgkmcnt(7)
	v_fma_f32 v37, v28, v38, 0
	v_fmac_f32_e32 v37, v29, v39
	v_fmac_f32_e32 v37, v30, v40
	v_fmac_f32_e32 v37, v31, v41
	s_waitcnt lgkmcnt(6)
	v_fmac_f32_e32 v37, v32, v42
	v_fmac_f32_e32 v37, v33, v43
	v_fmac_f32_e32 v37, v34, v44
	v_fmac_f32_e32 v37, v35, v45
	s_waitcnt lgkmcnt(5)
	v_fmac_f32_e32 v37, v18, v136
	v_fmac_f32_e32 v37, v19, v137
	v_fmac_f32_e32 v37, v20, v138
	v_fmac_f32_e32 v37, v21, v139
	s_waitcnt lgkmcnt(4)
	v_fmac_f32_e32 v37, v22, v140
	v_fmac_f32_e32 v37, v23, v141
	v_fmac_f32_e32 v37, v24, v142
	v_fmac_f32_e32 v37, v25, v143
	s_waitcnt lgkmcnt(3)
	v_fmac_f32_e32 v37, v17, v144
	v_fmac_f32_e32 v37, v16, v145
	v_fmac_f32_e32 v37, v15, v146
	v_fmac_f32_e32 v37, v14, v147
	s_waitcnt lgkmcnt(2)
	v_fmac_f32_e32 v37, v10, v148
	v_fmac_f32_e32 v37, v11, v149
	v_fmac_f32_e32 v37, v12, v150
	v_fmac_f32_e32 v37, v13, v151
	s_waitcnt lgkmcnt(1)
	v_fmac_f32_e32 v37, v9, v152
	v_fmac_f32_e32 v37, v8, v153
	v_fmac_f32_e32 v37, v7, v154
	v_fmac_f32_e32 v37, v6, v155
	s_waitcnt lgkmcnt(0)
	v_fmac_f32_e32 v37, v5, v156
	v_fmac_f32_e32 v37, v4, v157
	v_fmac_f32_e32 v37, v3, v158
	v_fmac_f32_e32 v37, v2, v159
	v_mov_b32_e32 v38, v37
	s_nop 1
	v_permlane32_swap_b32_e32 v37, v38
	v_add_f32_e32 v37, v37, v38
.LBB0_3019:
	s_cmpk_lt_u32 s56, 0x200
	s_cselect_b64 s[38:39], -1, 0
	s_cmpk_gt_u32 s56, 0x1ff
	s_cbranch_scc1 .LBB0_3021
	ds_read_b128 v[38:41], v163 offset:1280
	ds_read_b128 v[42:45], v163 offset:1296
	ds_read_b128 v[136:139], v163 offset:1344
	ds_read_b128 v[140:143], v163 offset:1360
	ds_read_b128 v[144:147], v163 offset:1408
	ds_read_b128 v[148:151], v163 offset:1424
	ds_read_b128 v[152:155], v163 offset:1472
	ds_read_b128 v[156:159], v163 offset:1488
	s_waitcnt lgkmcnt(7)
	v_fma_f32 v36, v28, v38, 0
	v_fmac_f32_e32 v36, v29, v39
	v_fmac_f32_e32 v36, v30, v40
	v_fmac_f32_e32 v36, v31, v41
	s_waitcnt lgkmcnt(6)
	v_fmac_f32_e32 v36, v32, v42
	v_fmac_f32_e32 v36, v33, v43
	v_fmac_f32_e32 v36, v34, v44
	v_fmac_f32_e32 v36, v35, v45
	s_waitcnt lgkmcnt(5)
	v_fmac_f32_e32 v36, v18, v136
	v_fmac_f32_e32 v36, v19, v137
	v_fmac_f32_e32 v36, v20, v138
	v_fmac_f32_e32 v36, v21, v139
	s_waitcnt lgkmcnt(4)
	v_fmac_f32_e32 v36, v22, v140
	v_fmac_f32_e32 v36, v23, v141
	v_fmac_f32_e32 v36, v24, v142
	v_fmac_f32_e32 v36, v25, v143
	s_waitcnt lgkmcnt(3)
	v_fmac_f32_e32 v36, v17, v144
	v_fmac_f32_e32 v36, v16, v145
	v_fmac_f32_e32 v36, v15, v146
	v_fmac_f32_e32 v36, v14, v147
	s_waitcnt lgkmcnt(2)
	v_fmac_f32_e32 v36, v10, v148
	v_fmac_f32_e32 v36, v11, v149
	v_fmac_f32_e32 v36, v12, v150
	v_fmac_f32_e32 v36, v13, v151
	s_waitcnt lgkmcnt(1)
	v_fmac_f32_e32 v36, v9, v152
	v_fmac_f32_e32 v36, v8, v153
	v_fmac_f32_e32 v36, v7, v154
	v_fmac_f32_e32 v36, v6, v155
	s_waitcnt lgkmcnt(0)
	v_fmac_f32_e32 v36, v5, v156
	v_fmac_f32_e32 v36, v4, v157
	v_fmac_f32_e32 v36, v3, v158
	v_fmac_f32_e32 v36, v2, v159
	v_mov_b32_e32 v38, v36
	s_nop 1
	v_permlane32_swap_b32_e32 v36, v38
	v_add_f32_e32 v36, v36, v38
.LBB0_3021:
	s_lshl_b32 s51, s57, 6
	s_cmpk_lt_u32 s56, 0x100
	v_mov_b32_e32 v197, 0
	s_cselect_b64 s[40:41], -1, 0
	s_cmpk_gt_u32 s56, 0xff
	v_mov_b32_e32 v38, 0
	s_cbranch_scc1 .LBB0_3023
	ds_read_b128 v[38:41], v163 offset:1536
	ds_read_b128 v[42:45], v163 offset:1552
	ds_read_b128 v[136:139], v163 offset:1600
	ds_read_b128 v[140:143], v163 offset:1616
	ds_read_b128 v[144:147], v163 offset:1664
	ds_read_b128 v[148:151], v163 offset:1680
	ds_read_b128 v[152:155], v163 offset:1728
	ds_read_b128 v[156:159], v163 offset:1744
	s_waitcnt lgkmcnt(7)
	v_fma_f32 v38, v28, v38, 0
	v_fmac_f32_e32 v38, v29, v39
	v_fmac_f32_e32 v38, v30, v40
	v_fmac_f32_e32 v38, v31, v41
	s_waitcnt lgkmcnt(6)
	v_fmac_f32_e32 v38, v32, v42
	v_fmac_f32_e32 v38, v33, v43
	v_fmac_f32_e32 v38, v34, v44
	v_fmac_f32_e32 v38, v35, v45
	s_waitcnt lgkmcnt(5)
	v_fmac_f32_e32 v38, v18, v136
	v_fmac_f32_e32 v38, v19, v137
	v_fmac_f32_e32 v38, v20, v138
	v_fmac_f32_e32 v38, v21, v139
	s_waitcnt lgkmcnt(4)
	v_fmac_f32_e32 v38, v22, v140
	v_fmac_f32_e32 v38, v23, v141
	v_fmac_f32_e32 v38, v24, v142
	v_fmac_f32_e32 v38, v25, v143
	s_waitcnt lgkmcnt(3)
	v_fmac_f32_e32 v38, v17, v144
	v_fmac_f32_e32 v38, v16, v145
	v_fmac_f32_e32 v38, v15, v146
	v_fmac_f32_e32 v38, v14, v147
	s_waitcnt lgkmcnt(2)
	v_fmac_f32_e32 v38, v10, v148
	v_fmac_f32_e32 v38, v11, v149
	v_fmac_f32_e32 v38, v12, v150
	v_fmac_f32_e32 v38, v13, v151
	s_waitcnt lgkmcnt(1)
	v_fmac_f32_e32 v38, v9, v152
	v_fmac_f32_e32 v38, v8, v153
	v_fmac_f32_e32 v38, v7, v154
	v_fmac_f32_e32 v38, v6, v155
	s_waitcnt lgkmcnt(0)
	v_fmac_f32_e32 v38, v5, v156
	v_fmac_f32_e32 v38, v4, v157
	v_fmac_f32_e32 v38, v3, v158
	v_fmac_f32_e32 v38, v2, v159
	v_mov_b32_e32 v2, v38
	s_nop 1
	v_permlane32_swap_b32_e32 v38, v2
	v_add_f32_e32 v38, v38, v2
